# wave 0 also requests its share of the first MoE unit's weight tiles, right after its grid handshake (before the barrier's closing s_barrier)
# baseline (speedup 1.0000x reference)
; #define GAS __attribute__((address_space(1)))
; #define MS_WLOAD(set, t) do { _Pragma("unroll") for (int r_ = 0; r_ < 4; ++r_) wr[set][r_] = __builtin_bit_cast(f32x4, __builtin_amdgcn_raw_buffer_load_b128(wrs, (int)wvo + r_ * LDW * 4, MS_CL(t) * (64 * LDW * 4), 0)); } while (0)
; #define MS_WCOMMIT(set, bufi) do { LAS unsigned char* wb_ = lds + (bufi) * MS_TILE; _Pragma("unroll") for (int i_ = 0; i_ < 4; ++i_) { \
;             u32x2 p_; p_.x = pk2(wr[set][0][i_], wr[set][1][i_]); p_.y = pk2(wr[set][2][i_], wr[set][3][i_]); \
;             *(LAS u32x2*)(wb_ + ((i_ < 2) ? lw0 : lw1) + i_ * 128) = p_; } } while (0)
; #define MS_XSLOAD(t) do { _Pragma("unroll") for (int i_ = 0; i_ < 6; ++i_) xs[i_] = __builtin_bit_cast(bf16x8, __builtin_amdgcn_raw_buffer_load_b128(xrs, (int)xso[i_], MS_CL(t) * 128, 0)); } while (0)
;     ...
;     const int half = wave & 1, nb16 = lane & 15, kb = 4 * (wave >> 1) + (lane >> 4);
;     const int tk = lane & 15, q = lane >> 4;
;     const GAS char* wmat = (const GAS char*)((MODE == 0) ? (half ? a.inp(I_WEU) : a.inp(I_WEG)) : a.inp(I_WED));
;     const unsigned wvo = (unsigned)((4 * kb * LDW + 4 * nb16) * 4);
;     const int lw0 = (64 * half + 4 * nb16) * 128 + (((kb >> 1) ^ ((2 * nb16) & 7)) << 4) + (kb & 1) * 8, lw1 = lw0 ^ 16;
;     const int rd_g = (tk >> 1) & 7;
;     for (int vb = bid; vb < NEXP * NSLAB; vb += G) {
;         const int xcd = vb & 7, idx = vb >> 3; const int e = xcd * 8 + idx / NSLAB, slab = idx % NSLAB;
;         const int M = __builtin_amdgcn_readfirstlane(lc[LC_CNT / 4 + e]), row0 = __builtin_amdgcn_readfirstlane(lc[LC_PSTART / 4 + e]);
;         const size_t wuo = (MODE == 0) ? ((size_t)(l * NEXP + e) * D * DEXP + slab * 64) * 4 : ((size_t)(l * NEXP + e) * DEXP * D + slab * 128 + 64 * half) * 4;
;         const __amdgpu_buffer_rsrc_t wrs = __builtin_amdgcn_make_buffer_rsrc((void*)(wmat + wuo), 0, KD * LDW * 4, 0x00020000);
;     ...
;             MS_XSLOAD(0); MS_WLOAD(0, 0); MS_WLOAD(1, 1);
;             MS_WCOMMIT(0, 0); MS_WLOAD(0, 2);
.LBB0_1707:
	s_or_b64 exec, exec, s[4:5]
	v_readfirstlane_b32 s88, v0
	s_lshr_b32 s88, s88, 6
	s_cmp_eq_u32 s88, 0
	s_cbranch_scc0 .Lpfk0_end
	s_cmpk_gt_i32 s72, 0x1ff
	s_cbranch_scc1 .Lpfk0_end
	s_and_b32 s81, s88, 1
	s_lshl_b32 s81, s81, 3
	s_add_i32 s81, s81, 0xe8
	s_load_dwordx2 s[70:71], s[74:75], s81
	v_readlane_b32 s82, v255, 30
	s_lshl_b32 s82, s82, 6
	s_and_b32 s84, s72, 7
	s_lshl_b32 s84, s84, 3
	s_lshr_b32 s85, s72, 6
	s_add_i32 s84, s84, s85
	s_add_i32 s84, s84, s82
	s_lshr_b32 s85, s72, 3
	s_and_b32 s85, s85, 7
	s_lshl_b32 s85, s85, 8
	s_lshr_b32 s86, s84, 10
	s_lshl_b32 s84, s84, 22
	s_or_b32 s84, s84, s85
	s_waitcnt lgkmcnt(0)
	s_add_u32 s84, s70, s84
	s_addc_u32 s85, s71, s86
	s_and_b32 s85, s85, 0xffff
	s_mov_b32 s86, 0x7ffffff0
	s_mov_b32 s87, 0x20000
	v_and_b32_e32 v250, 15, v0
	v_lshlrev_b32_e32 v250, 4, v250
	v_bfe_u32 v251, v0, 4, 2
	s_lshr_b32 s81, s88, 1
	s_lshl_b32 s81, s81, 2
	v_add_u32_e32 v251, s81, v251
	v_lshl_or_b32 v250, v251, 13, v250
	v_or_b32_e32 v251, 0x800, v250
	v_or_b32_e32 v252, 0x1000, v250
	v_or_b32_e32 v253, 0x1800, v250
	buffer_load_dwordx4 v[26:29], v250, s[84:87], 0 offen nt
	buffer_load_dwordx4 v[30:33], v251, s[84:87], 0 offen nt
	buffer_load_dwordx4 v[34:37], v252, s[84:87], 0 offen nt
	buffer_load_dwordx4 v[38:41], v253, s[84:87], 0 offen nt
	s_mov_b32 s81, 0x20000
	buffer_load_dwordx4 v[74:77], v250, s[84:87], s81 offen nt
	buffer_load_dwordx4 v[78:81], v251, s[84:87], s81 offen nt
	buffer_load_dwordx4 v[82:85], v252, s[84:87], s81 offen nt
	buffer_load_dwordx4 v[86:89], v253, s[84:87], s81 offen nt
	s_mov_b32 s81, 0x40000
	buffer_load_dwordx4 v[96:99], v250, s[84:87], s81 offen nt
	buffer_load_dwordx4 v[100:103], v251, s[84:87], s81 offen nt
	buffer_load_dwordx4 v[104:107], v252, s[84:87], s81 offen nt
	buffer_load_dwordx4 v[108:111], v253, s[84:87], s81 offen nt
	s_mov_b32 s67, 1
.Lpfk0_end:
	s_waitcnt lgkmcnt(0)
	s_barrier
.LBB0_1708:
	s_cmp_le_i32 s76, s0
	s_waitcnt lgkmcnt(0)
	s_cselect_b64 s[2:3], -1, 0
	s_cmp_lt_i32 s0, s77
	s_cselect_b64 s[0:1], -1, 0
	s_and_b64 s[0:1], s[2:3], s[0:1]
	s_mov_b64 s[2:3], -1
	s_and_b64 vcc, exec, s[0:1]
	s_cbranch_vccnz .LBB0_1710
	v_readlane_b32 s0, v255, 32
	s_add_i32 s0, s0, 10
	s_mov_b64 s[2:3], 0

; #define GAS __attribute__((address_space(1)))
; #define MS_WLOAD(set, t) do { _Pragma("unroll") for (int r_ = 0; r_ < 4; ++r_) wr[set][r_] = __builtin_bit_cast(f32x4, __builtin_amdgcn_raw_buffer_load_b128(wrs, (int)wvo + r_ * LDW * 4, MS_CL(t) * (64 * LDW * 4), 0)); } while (0)
; #define MS_WCOMMIT(set, bufi) do { LAS unsigned char* wb_ = lds + (bufi) * MS_TILE; _Pragma("unroll") for (int i_ = 0; i_ < 4; ++i_) { \
;             u32x2 p_; p_.x = pk2(wr[set][0][i_], wr[set][1][i_]); p_.y = pk2(wr[set][2][i_], wr[set][3][i_]); \
;             *(LAS u32x2*)(wb_ + ((i_ < 2) ? lw0 : lw1) + i_ * 128) = p_; } } while (0)
; #define MS_XSLOAD(t) do { _Pragma("unroll") for (int i_ = 0; i_ < 6; ++i_) xs[i_] = __builtin_bit_cast(bf16x8, __builtin_amdgcn_raw_buffer_load_b128(xrs, (int)xso[i_], MS_CL(t) * 128, 0)); } while (0)
;     ...
;     const int half = wave & 1, nb16 = lane & 15, kb = 4 * (wave >> 1) + (lane >> 4);
;     const int tk = lane & 15, q = lane >> 4;
;     const GAS char* wmat = (const GAS char*)((MODE == 0) ? (half ? a.inp(I_WEU) : a.inp(I_WEG)) : a.inp(I_WED));
;     const unsigned wvo = (unsigned)((4 * kb * LDW + 4 * nb16) * 4);
;     const int lw0 = (64 * half + 4 * nb16) * 128 + (((kb >> 1) ^ ((2 * nb16) & 7)) << 4) + (kb & 1) * 8, lw1 = lw0 ^ 16;
;     const int rd_g = (tk >> 1) & 7;
;     for (int vb = bid; vb < NEXP * NSLAB; vb += G) {
;         const int xcd = vb & 7, idx = vb >> 3; const int e = xcd * 8 + idx / NSLAB, slab = idx % NSLAB;
;         const int M = __builtin_amdgcn_readfirstlane(lc[LC_CNT / 4 + e]), row0 = __builtin_amdgcn_readfirstlane(lc[LC_PSTART / 4 + e]);
;         const size_t wuo = (MODE == 0) ? ((size_t)(l * NEXP + e) * D * DEXP + slab * 64) * 4 : ((size_t)(l * NEXP + e) * DEXP * D + slab * 128 + 64 * half) * 4;
;         const __amdgpu_buffer_rsrc_t wrs = __builtin_amdgcn_make_buffer_rsrc((void*)(wmat + wuo), 0, KD * LDW * 4, 0x00020000);
;     ...
;             MS_XSLOAD(0); MS_WLOAD(0, 0); MS_WLOAD(1, 1);
;             MS_WCOMMIT(0, 0); MS_WLOAD(0, 2);
.LBB0_1776:
	s_or_b64 exec, exec, s[4:5]
	v_readfirstlane_b32 s88, v0
	s_lshr_b32 s88, s88, 6
	s_cmp_eq_u32 s88, 0
	s_cbranch_scc0 .Lpfl0_end
	s_cmpk_gt_i32 s72, 0x3ff
	s_cbranch_scc1 .Lpfl0_end
	s_load_dwordx2 s[70:71], s[74:75], 0xf8
	v_readlane_b32 s82, v255, 30
	s_lshl_b32 s82, s82, 6
	s_and_b32 s84, s72, 7
	s_lshl_b32 s84, s84, 3
	s_lshr_b32 s85, s72, 7
	s_add_i32 s84, s84, s85
	s_add_i32 s84, s84, s82
	s_lshr_b32 s85, s72, 3
	s_and_b32 s85, s85, 15
	s_lshl_b32 s85, s85, 9
	s_and_b32 s81, s88, 1
	s_lshl_b32 s81, s81, 8
	s_or_b32 s85, s85, s81
	s_lshr_b32 s86, s84, 10
	s_lshl_b32 s84, s84, 22
	s_or_b32 s84, s84, s85
	s_waitcnt lgkmcnt(0)
	s_add_u32 s84, s70, s84
	s_addc_u32 s85, s71, s86
	s_and_b32 s85, s85, 0xffff
	s_mov_b32 s86, 0x7ffffff0
	s_mov_b32 s87, 0x20000
	v_and_b32_e32 v250, 15, v0
	v_lshlrev_b32_e32 v250, 4, v250
	v_bfe_u32 v251, v0, 4, 2
	s_lshr_b32 s81, s88, 1
	s_lshl_b32 s81, s81, 2
	v_add_u32_e32 v251, s81, v251
	v_lshl_or_b32 v250, v251, 15, v250
	v_or_b32_e32 v251, 0x2000, v250
	v_or_b32_e32 v252, 0x4000, v250
	v_or_b32_e32 v253, 0x6000, v250
	buffer_load_dwordx4 v[52:55], v250, s[84:87], 0 offen nt
	buffer_load_dwordx4 v[56:59], v251, s[84:87], 0 offen nt
	buffer_load_dwordx4 v[60:63], v252, s[84:87], 0 offen nt
	buffer_load_dwordx4 v[64:67], v253, s[84:87], 0 offen nt
	s_mov_b32 s81, 0x80000
	buffer_load_dwordx4 v[120:123], v250, s[84:87], s81 offen nt
	buffer_load_dwordx4 v[128:131], v251, s[84:87], s81 offen nt
	buffer_load_dwordx4 v[124:127], v252, s[84:87], s81 offen nt
	buffer_load_dwordx4 v[132:135], v253, s[84:87], s81 offen nt
	s_mov_b32 s81, 0x100000
	buffer_load_dwordx4 v[136:139], v250, s[84:87], s81 offen nt
	buffer_load_dwordx4 v[140:143], v251, s[84:87], s81 offen nt
	buffer_load_dwordx4 v[144:147], v252, s[84:87], s81 offen nt
	buffer_load_dwordx4 v[148:151], v253, s[84:87], s81 offen nt
	s_mov_b32 s67, 1
.Lpfl0_end:
	s_waitcnt lgkmcnt(0)
	s_barrier
.LBB0_1777:
	s_cmp_gt_i32 s76, s0
	s_cselect_b64 s[2:3], -1, 0
	s_cmp_ge_i32 s0, s77
	s_cselect_b64 s[0:1], -1, 0
	s_or_b64 s[0:1], s[2:3], s[0:1]
	s_and_b64 vcc, exec, s[0:1]
	s_cbranch_vccz .LBB0_1778
	s_getpc_b64 s[98:99]
